# RTO unit tail: 32 retention-state loads batched (on top of rtp fix)
# speedup vs baseline: 1.0066x; 1.0008x over previous
.LBB0_727:
	s_or_b64 exec, exec, s[6:7]
	s_cmp_gt_i32 s10, -1
	s_cselect_b32 s0, 19, 1
	s_lshl_b32 s6, s14, 3
	s_lshl_b32 s7, s15, 1
	s_or_b32 s6, s7, s6
	s_mul_i32 s14, s6, 18
	s_add_i32 s6, s14, s11
	s_ashr_i32 s7, s6, 31
	s_lshl_b64 s[6:7], s[6:7], 15
	s_add_u32 s6, s12, s6
	s_addc_u32 s7, s13, s7
	v_ashrrev_i32_e32 v147, 2, v143
	v_lshl_add_u64 v[48:49], s[6:7], 0, v[96:97]
	s_movk_i32 s6, 0xffc0
	v_mul_f32_e32 v0, v0, v18
	v_and_or_b32 v60, v147, s6, v16
	v_mul_f32_e32 v1, v1, v19
	v_cvt_pk_bf16_f32 v138, v0, v1
	v_lshlrev_b32_e32 v0, 7, v60
	v_ashrrev_i32_e32 v1, 31, v0
	v_mul_f32_e32 v8, v8, v26
	v_mul_f32_e32 v9, v9, v27
	v_lshlrev_b64 v[26:27], 1, v[0:1]
	v_lshl_add_u64 v[54:55], v[48:49], 0, v[26:27]
	v_mul_f32_e32 v2, v2, v20
	v_mul_f32_e32 v3, v3, v21
	v_mul_f32_e32 v4, v4, v22
	v_mul_f32_e32 v5, v5, v23
	v_mul_f32_e32 v6, v6, v24
	v_mul_f32_e32 v7, v7, v25
	v_mul_f32_e32 v10, v10, v28
	v_mul_f32_e32 v11, v11, v29
	v_mul_f32_e32 v12, v12, v30
	v_mul_f32_e32 v13, v13, v31
	v_mul_f32_e32 v14, v14, v32
	v_mul_f32_e32 v15, v15, v33
	v_cvt_pk_bf16_f32 v139, v2, v3
	v_cvt_pk_bf16_f32 v140, v4, v5
	v_cvt_pk_bf16_f32 v141, v6, v7
	v_cvt_pk_bf16_f32 v134, v8, v9
	v_cvt_pk_bf16_f32 v135, v10, v11
	v_cvt_pk_bf16_f32 v136, v12, v13
	v_cvt_pk_bf16_f32 v137, v14, v15
	global_load_dwordx4 v[160:163], v[54:55], off
	global_load_dwordx4 v[164:167], v[54:55], off offset:32
	global_load_dwordx4 v[168:171], v[54:55], off offset:64
	global_load_dwordx4 v[172:175], v[54:55], off offset:96
	global_load_dwordx4 v[176:179], v[54:55], off offset:128
	global_load_dwordx4 v[180:183], v[54:55], off offset:160
	global_load_dwordx4 v[184:187], v[54:55], off offset:192
	global_load_dwordx4 v[188:191], v[54:55], off offset:224
	s_movk_i32 s11, 0x110
	v_lshlrev_b32_e32 v156, 1, v17
	v_mul_lo_u32 v0, v60, s11
	v_add3_u32 v61, s3, v0, v156
	ds_read2_b64 v[0:3], v61 offset1:2
	ds_read2_b64 v[22:25], v61 offset0:4 offset1:6
	s_waitcnt lgkmcnt(1)
	v_mfma_f32_32x32x16_bf16 v[0:15], v[0:3], v[110:113], 0
	s_sub_i32 s0, s0, s10
	s_add_i32 s0, s0, s14
	s_add_i32 s0, s0, 16
	s_lshl_b64 s[6:7], s[0:1], 15
	s_add_u32 s6, s12, s6
	s_addc_u32 s7, s13, s7
	v_lshl_add_u64 v[56:57], s[6:7], 0, v[96:97]
	s_waitcnt lgkmcnt(0)
	v_mfma_f32_32x32x16_bf16 v[0:15], v[22:25], v[114:117], v[0:15]
	ds_read2_b64 v[22:25], v61 offset0:8 offset1:10
	v_lshl_add_u64 v[58:59], v[56:57], 0, v[26:27]
	global_load_dwordx4 v[192:195], v[58:59], off
	global_load_dwordx4 v[196:199], v[58:59], off offset:32
	global_load_dwordx4 v[200:203], v[58:59], off offset:64
	global_load_dwordx4 v[204:207], v[58:59], off offset:96
	global_load_dwordx4 v[208:211], v[58:59], off offset:128
	global_load_dwordx4 v[220:223], v[58:59], off offset:160
	global_load_dwordx4 v[224:227], v[58:59], off offset:192
	global_load_dwordx4 v[228:231], v[58:59], off offset:224
	v_or_b32_e32 v157, 32, v60
	v_lshlrev_b32_e32 v54, 7, v157
	v_ashrrev_i32_e32 v55, 31, v54
	v_lshlrev_b64 v[54:55], 1, v[54:55]
	v_lshl_add_u64 v[152:153], v[48:49], 0, v[54:55]
	v_lshl_add_u64 v[154:155], v[56:57], 0, v[54:55]
	global_load_dwordx4 v[232:235], v[152:153], off
	global_load_dwordx4 v[236:239], v[154:155], off
	global_load_dwordx4 v[244:247], v[152:153], off offset:32
	global_load_dwordx4 v[248:251], v[154:155], off offset:32
	global_load_dwordx4 v[214:217], v[152:153], off offset:64
	s_movk_i32 s10, 0x204
	s_lshl_b32 s0, s2, 1
	s_waitcnt lgkmcnt(0)
	v_mfma_f32_32x32x16_bf16 v[0:15], v[22:25], v[122:125], v[0:15]
	s_waitcnt vmcnt(20)
	v_mfma_f32_32x32x16_bf16 v[16:31], v[160:163], v[64:67], 0
	global_load_dwordx4 v[160:163], v[154:155], off offset:64
	s_waitcnt vmcnt(20)
	v_mfma_f32_32x32x16_bf16 v[16:31], v[164:167], v[106:109], v[16:31]
	global_load_dwordx4 v[164:167], v[152:153], off offset:96
	s_waitcnt vmcnt(14)
	v_mfma_f32_32x32x16_bf16 v[32:47], v[192:195], v[64:67], 0
	global_load_dwordx4 v[192:195], v[154:155], off offset:96
	s_waitcnt vmcnt(14)
	v_mfma_f32_32x32x16_bf16 v[32:47], v[196:199], v[106:109], v[32:47]
	global_load_dwordx4 v[196:199], v[152:153], off offset:128
	s_waitcnt vmcnt(22)
	v_mfma_f32_32x32x16_bf16 v[16:31], v[168:171], v[102:105], v[16:31]
	global_load_dwordx4 v[168:171], v[154:155], off offset:128
	s_waitcnt vmcnt(15)
	v_mfma_f32_32x32x16_bf16 v[32:47], v[200:203], v[102:105], v[32:47]
	global_load_dwordx4 v[200:203], v[152:153], off offset:160
	s_waitcnt vmcnt(23)
	v_mfma_f32_32x32x16_bf16 v[16:31], v[172:175], v[92:95], v[16:31]
	global_load_dwordx4 v[172:175], v[154:155], off offset:160
	s_waitcnt vmcnt(16)
	v_mfma_f32_32x32x16_bf16 v[32:47], v[204:207], v[92:95], v[32:47]
	global_load_dwordx4 v[204:207], v[152:153], off offset:192
	s_waitcnt vmcnt(24)
	v_mfma_f32_32x32x16_bf16 v[16:31], v[176:179], v[88:91], v[16:31]
	global_load_dwordx4 v[176:179], v[154:155], off offset:192
	s_waitcnt vmcnt(17)
	v_mfma_f32_32x32x16_bf16 v[32:47], v[208:211], v[88:91], v[32:47]
	global_load_dwordx4 v[208:211], v[152:153], off offset:224
	s_waitcnt vmcnt(25)
	v_mfma_f32_32x32x16_bf16 v[16:31], v[180:183], v[84:87], v[16:31]
	global_load_dwordx4 v[180:183], v[154:155], off offset:224
	s_waitcnt vmcnt(18)
	v_mfma_f32_32x32x16_bf16 v[32:47], v[220:223], v[84:87], v[32:47]
	s_waitcnt vmcnt(25)
	v_mfma_f32_32x32x16_bf16 v[16:31], v[184:187], v[80:83], v[16:31]
	s_waitcnt vmcnt(17)
	v_mfma_f32_32x32x16_bf16 v[32:47], v[224:227], v[80:83], v[32:47]
	s_waitcnt vmcnt(24)
	v_mfma_f32_32x32x16_bf16 v[16:31], v[188:191], v[98:101], v[16:31]
	s_waitcnt vmcnt(16)
	v_mfma_f32_32x32x16_bf16 v[32:47], v[228:231], v[98:101], v[32:47]
	ds_read2_b64 v[50:53], v61 offset0:12 offset1:14
	s_waitcnt lgkmcnt(0)
	v_mfma_f32_32x32x16_bf16 v[0:15], v[50:53], v[118:121], v[0:15]
	ds_read2_b64 v[50:53], v61 offset0:16 offset1:18
	s_waitcnt lgkmcnt(0)
	v_mfma_f32_32x32x16_bf16 v[0:15], v[50:53], v[130:133], v[0:15]
	ds_read2_b64 v[50:53], v61 offset0:20 offset1:22
	s_waitcnt lgkmcnt(0)
	v_mfma_f32_32x32x16_bf16 v[0:15], v[50:53], v[126:129], v[0:15]
	ds_read2_b64 v[50:53], v61 offset0:24 offset1:26
	s_waitcnt lgkmcnt(0)
	v_mfma_f32_32x32x16_bf16 v[0:15], v[50:53], v[138:141], v[0:15]
	ds_read2_b64 v[50:53], v61 offset0:28 offset1:30
	s_waitcnt lgkmcnt(0)
	v_mfma_f32_32x32x16_bf16 v[0:15], v[50:53], v[134:137], v[0:15]
	s_waitcnt vmcnt(15)
	v_mfma_f32_32x32x16_bf16 v[48:63], v[232:235], v[64:67], 0
	s_waitcnt vmcnt(13)
	v_mfma_f32_32x32x16_bf16 v[48:63], v[244:247], v[106:109], v[48:63]
	s_waitcnt vmcnt(14)
	v_mfma_f32_32x32x16_bf16 v[64:79], v[236:239], v[64:67], 0
	s_waitcnt vmcnt(12)
	v_mfma_f32_32x32x16_bf16 v[64:79], v[248:251], v[106:109], v[64:79]
	s_waitcnt vmcnt(11)
	v_mfma_f32_32x32x16_bf16 v[48:63], v[214:217], v[102:105], v[48:63]
	s_waitcnt vmcnt(10)
	v_mfma_f32_32x32x16_bf16 v[64:79], v[160:163], v[102:105], v[64:79]
	s_waitcnt vmcnt(9)
	v_mfma_f32_32x32x16_bf16 v[48:63], v[164:167], v[92:95], v[48:63]
	s_waitcnt vmcnt(8)
	v_mfma_f32_32x32x16_bf16 v[64:79], v[192:195], v[92:95], v[64:79]
	s_waitcnt vmcnt(7)
	v_mfma_f32_32x32x16_bf16 v[48:63], v[196:199], v[88:91], v[48:63]
	s_waitcnt vmcnt(6)
	v_mfma_f32_32x32x16_bf16 v[64:79], v[168:171], v[88:91], v[64:79]
	s_waitcnt vmcnt(5)
	v_mfma_f32_32x32x16_bf16 v[48:63], v[200:203], v[84:87], v[48:63]
	s_waitcnt vmcnt(4)
	v_mfma_f32_32x32x16_bf16 v[64:79], v[172:175], v[84:87], v[64:79]
	s_waitcnt vmcnt(3)
	v_mfma_f32_32x32x16_bf16 v[48:63], v[204:207], v[80:83], v[48:63]
	s_waitcnt vmcnt(2)
	v_mfma_f32_32x32x16_bf16 v[64:79], v[176:179], v[80:83], v[64:79]
	v_mul_lo_u32 v84, v157, s11
	v_add3_u32 v148, s3, v84, v156
	ds_read2_b64 v[106:109], v148 offset0:4 offset1:6
	s_waitcnt vmcnt(1)
	v_mfma_f32_32x32x16_bf16 v[48:63], v[208:211], v[98:101], v[48:63]
	ds_read2_b64 v[80:83], v148 offset1:2
	s_waitcnt lgkmcnt(0)
	v_mfma_f32_32x32x16_bf16 v[80:95], v[80:83], v[110:113], 0
	ds_read2_b64 v[110:113], v148 offset0:12 offset1:14
	v_mfma_f32_32x32x16_bf16 v[80:95], v[106:109], v[114:117], v[80:95]
	ds_read2_b64 v[106:109], v148 offset0:8 offset1:10
	v_add_u32_e32 v114, 1, v146
	s_waitcnt lgkmcnt(0)
	v_mfma_f32_32x32x16_bf16 v[80:95], v[106:109], v[122:125], v[80:95]
	v_cvt_f32_ubyte0_e32 v106, v114
	v_mul_f32_e32 v106, v144, v106
	v_exp_f32_e32 v122, v106
	v_sub_u32_e32 v106, 0x80, v146
	v_cvt_f32_ubyte0_e32 v106, v106
	v_mul_f32_e32 v114, v145, v106
	ds_read2_b64 v[106:109], v148 offset0:16 offset1:18
	v_mfma_f32_32x32x16_bf16 v[80:95], v[110:113], v[118:121], v[80:95]
	v_exp_f32_e32 v124, v114
	ds_read2_b64 v[110:113], v148 offset0:20 offset1:22
	ds_read2_b64 v[114:117], v148 offset0:24 offset1:26
	ds_read2_b64 v[118:121], v148 offset0:28 offset1:30
	v_pk_fma_f32 v[0:1], v[122:123], v[16:17], v[0:1] op_sel_hi:[0,1,1]
	s_waitcnt lgkmcnt(0)
	v_pk_fma_f32 v[0:1], v[124:125], v[32:33], v[0:1] op_sel_hi:[0,1,1]
	s_barrier
	v_mfma_f32_32x32x16_bf16 v[80:95], v[106:109], v[130:133], v[80:95]
	v_mad_u32_u24 v106, v146, s10, 0
	v_and_b32_e32 v107, 0xffffff00, v143
	v_add3_u32 v96, v106, v107, v96
	ds_write2_b32 v96, v0, v1 offset1:1
	v_fma_f32 v0, v122, v18, v2
	v_fma_f32 v1, v122, v19, v3
	v_pk_fma_f32 v[0:1], v[124:125], v[34:35], v[0:1] op_sel_hi:[0,1,1]
	ds_write2_b32 v96, v0, v1 offset0:2 offset1:3
	v_mfma_f32_32x32x16_bf16 v[80:95], v[110:113], v[126:129], v[80:95]
	v_fma_f32 v0, v122, v20, v4
	v_fma_f32 v1, v122, v21, v5
	v_fma_f32 v0, v124, v36, v0
	v_fma_f32 v1, v124, v37, v1
	ds_write2_b32 v96, v0, v1 offset0:8 offset1:9
	v_pk_fma_f32 v[0:1], v[122:123], v[22:23], v[6:7] op_sel_hi:[0,1,1]
	v_pk_fma_f32 v[0:1], v[124:125], v[38:39], v[0:1] op_sel_hi:[0,1,1]
	ds_write2_b32 v96, v0, v1 offset0:10 offset1:11
	v_pk_fma_f32 v[0:1], v[122:123], v[24:25], v[8:9] op_sel_hi:[0,1,1]
	v_mfma_f32_32x32x16_bf16 v[80:95], v[114:117], v[138:141], v[80:95]
	v_fma_f32 v0, v124, v40, v0
	v_fma_f32 v1, v124, v41, v1
	ds_write2_b32 v96, v0, v1 offset0:16 offset1:17
	v_fma_f32 v0, v122, v26, v10
	v_fma_f32 v1, v122, v27, v11
	v_pk_fma_f32 v[0:1], v[124:125], v[42:43], v[0:1] op_sel_hi:[0,1,1]
	ds_write2_b32 v96, v0, v1 offset0:18 offset1:19
	v_pk_fma_f32 v[0:1], v[122:123], v[28:29], v[12:13] op_sel_hi:[0,1,1]
	v_pk_fma_f32 v[0:1], v[124:125], v[44:45], v[0:1] op_sel_hi:[0,1,1]
	v_mfma_f32_32x32x16_bf16 v[80:95], v[118:121], v[134:137], v[80:95]
	ds_write2_b32 v96, v0, v1 offset0:24 offset1:25
	v_fma_f32 v0, v122, v30, v14
	v_fma_f32 v1, v122, v31, v15
	v_fma_f32 v0, v124, v46, v0
	v_fma_f32 v1, v124, v47, v1
	ds_write2_b32 v96, v0, v1 offset0:26 offset1:27
	v_add_u32_e32 v36, s9, v147
	v_and_b32_e32 v2, 3, v142
	s_nop 3
	v_pk_fma_f32 v[0:1], v[122:123], v[48:49], v[80:81] op_sel_hi:[0,1,1]
	s_waitcnt vmcnt(0)
	v_mfma_f32_32x32x16_bf16 v[64:79], v[180:183], v[98:101], v[64:79]
	s_nop 11
	v_pk_fma_f32 v[0:1], v[124:125], v[64:65], v[0:1] op_sel_hi:[0,1,1]
	ds_write2_b32 v96, v0, v1 offset0:32 offset1:33
	v_pk_fma_f32 v[0:1], v[122:123], v[50:51], v[82:83] op_sel_hi:[0,1,1]
	v_pk_fma_f32 v[0:1], v[124:125], v[66:67], v[0:1] op_sel_hi:[0,1,1]
	ds_write2_b32 v96, v0, v1 offset0:34 offset1:35
	v_pk_fma_f32 v[0:1], v[122:123], v[52:53], v[84:85] op_sel_hi:[0,1,1]
	v_pk_fma_f32 v[0:1], v[124:125], v[68:69], v[0:1] op_sel_hi:[0,1,1]
	ds_write2_b32 v96, v0, v1 offset0:40 offset1:41
	v_pk_fma_f32 v[0:1], v[122:123], v[54:55], v[86:87] op_sel_hi:[0,1,1]
	v_pk_fma_f32 v[0:1], v[124:125], v[70:71], v[0:1] op_sel_hi:[0,1,1]
	ds_write2_b32 v96, v0, v1 offset0:42 offset1:43
	v_pk_fma_f32 v[0:1], v[122:123], v[56:57], v[88:89] op_sel_hi:[0,1,1]
	v_pk_fma_f32 v[0:1], v[124:125], v[72:73], v[0:1] op_sel_hi:[0,1,1]
	ds_write2_b32 v96, v0, v1 offset0:48 offset1:49
	v_pk_fma_f32 v[0:1], v[122:123], v[58:59], v[90:91] op_sel_hi:[0,1,1]
	v_pk_fma_f32 v[0:1], v[124:125], v[74:75], v[0:1] op_sel_hi:[0,1,1]
	ds_write2_b32 v96, v0, v1 offset0:50 offset1:51
	v_pk_fma_f32 v[0:1], v[122:123], v[60:61], v[92:93] op_sel_hi:[0,1,1]
	v_pk_fma_f32 v[0:1], v[124:125], v[76:77], v[0:1] op_sel_hi:[0,1,1]
	ds_write2_b32 v96, v0, v1 offset0:56 offset1:57
	v_pk_fma_f32 v[0:1], v[122:123], v[62:63], v[94:95] op_sel_hi:[0,1,1]
	v_pk_fma_f32 v[0:1], v[124:125], v[78:79], v[0:1] op_sel_hi:[0,1,1]
	ds_write2_b32 v96, v0, v1 offset0:58 offset1:59
	v_mov_b64_e32 v[0:1], s[84:85]
	v_mad_i64_i32 v[0:1], s[6:7], v36, s95, v[0:1]
	v_lshl_add_u64 v[0:1], v[0:1], 0, s[0:1]
	v_lshlrev_b32_e32 v96, 6, v2
	v_lshl_add_u64 v[10:11], v[0:1], 0, v[96:97]
	v_add_co_u32_e32 v0, vcc, s63, v10
	s_waitcnt lgkmcnt(0)
	s_nop 0
	v_addc_co_u32_e32 v1, vcc, 0, v11, vcc
	s_barrier
	global_load_dwordx4 v[24:27], v[0:1], off offset:2048
	v_lshlrev_b32_e32 v54, 7, v2
	global_load_dwordx4 v[28:31], v54, s[4:5]
	global_load_dwordx4 v[32:35], v54, s[4:5] offset:16
	v_mul_lo_u32 v0, v147, s10
	v_add3_u32 v0, 0, v0, v54
	ds_read2_b32 v[38:39], v0 offset1:1
	ds_read2_b32 v[40:41], v0 offset0:2 offset1:3
	ds_read2_b32 v[42:43], v0 offset0:4 offset1:5
	ds_read2_b32 v[44:45], v0 offset0:6 offset1:7
	ds_read2_b32 v[46:47], v0 offset0:8 offset1:9
	ds_read2_b32 v[48:49], v0 offset0:10 offset1:11
	ds_read2_b32 v[20:21], v0 offset0:12 offset1:13
	ds_read2_b32 v[18:19], v0 offset0:14 offset1:15
	ds_read2_b32 v[16:17], v0 offset0:16 offset1:17
	s_waitcnt lgkmcnt(8)
	v_mul_f32_e32 v37, v39, v39
	v_fmac_f32_e32 v37, v38, v38
	s_waitcnt lgkmcnt(7)
	v_fmac_f32_e32 v37, v40, v40
	v_fmac_f32_e32 v37, v41, v41
	s_waitcnt lgkmcnt(6)
	v_fmac_f32_e32 v37, v42, v42
	v_fmac_f32_e32 v37, v43, v43
	s_waitcnt lgkmcnt(5)
	v_fmac_f32_e32 v37, v44, v44
	v_fmac_f32_e32 v37, v45, v45
	s_waitcnt lgkmcnt(4)
	v_fmac_f32_e32 v37, v46, v46
	v_fmac_f32_e32 v37, v47, v47
	s_waitcnt lgkmcnt(3)
	v_fmac_f32_e32 v37, v48, v48
	v_fmac_f32_e32 v37, v49, v49
	s_waitcnt lgkmcnt(2)
	v_fmac_f32_e32 v37, v20, v20
	v_fmac_f32_e32 v37, v21, v21
	s_waitcnt lgkmcnt(1)
	v_fmac_f32_e32 v37, v18, v18
	v_fmac_f32_e32 v37, v19, v19
	ds_read2_b32 v[14:15], v0 offset0:18 offset1:19
	ds_read2_b32 v[12:13], v0 offset0:20 offset1:21
	ds_read2_b32 v[8:9], v0 offset0:22 offset1:23
	s_waitcnt lgkmcnt(3)
	v_fmac_f32_e32 v37, v16, v16
	v_fmac_f32_e32 v37, v17, v17
	s_waitcnt lgkmcnt(2)
	v_fmac_f32_e32 v37, v14, v14
	ds_read2_b32 v[6:7], v0 offset0:24 offset1:25
	v_fmac_f32_e32 v37, v15, v15
	s_waitcnt lgkmcnt(2)
	v_fmac_f32_e32 v37, v12, v12
	v_fmac_f32_e32 v37, v13, v13
	s_waitcnt lgkmcnt(1)
	v_fmac_f32_e32 v37, v8, v8
	ds_read2_b32 v[4:5], v0 offset0:26 offset1:27
	ds_read2_b32 v[2:3], v0 offset0:28 offset1:29
	ds_read2_b32 v[0:1], v0 offset0:30 offset1:31
	v_fmac_f32_e32 v37, v9, v9
	s_waitcnt lgkmcnt(3)
	v_pk_mul_f32 v[22:23], v[6:7], v[6:7]
	s_mov_b64 s[6:7], 0x1800
	v_add_f32_e32 v22, v37, v22
	v_add_f32_e32 v37, v22, v23
	s_waitcnt lgkmcnt(2)
	v_pk_mul_f32 v[22:23], v[4:5], v[4:5]
	v_lshl_add_u64 v[10:11], v[10:11], 0, s[6:7]
	v_add_f32_e32 v22, v37, v22
	v_add_f32_e32 v37, v22, v23
	s_waitcnt lgkmcnt(1)
	v_pk_mul_f32 v[22:23], v[2:3], v[2:3]
	s_mov_b64 s[6:7], 0x18b00400
	v_add_f32_e32 v22, v37, v22
	v_add_f32_e32 v37, v22, v23
	s_waitcnt lgkmcnt(0)
	v_pk_mul_f32 v[22:23], v[0:1], v[0:1]
	s_waitcnt vmcnt(2)
	v_lshlrev_b32_e32 v50, 16, v24
	v_add_f32_e32 v22, v37, v22
	v_add_f32_e32 v22, v22, v23
	s_waitcnt vmcnt(1)
	v_mov_b32_e32 v53, v28
	v_ashrrev_i32_e32 v37, 31, v36
	v_add_f32_dpp v22, v22, v22 quad_perm:[1,0,3,2] row_mask:0xf bank_mask:0xf bound_ctrl:1
	v_lshlrev_b64 v[36:37], 12, v[36:37]
	v_lshl_add_u64 v[36:37], s[96:97], 0, v[36:37]
	v_add_f32_dpp v22, v22, v22 quad_perm:[2,3,0,1] row_mask:0xf bank_mask:0xf bound_ctrl:1
	v_fmamk_f32 v22, v22, 0x3c000000, v213
	v_mul_f32_e32 v23, 0x4b800000, v22
	v_cmp_gt_f32_e32 vcc, s64, v22
	s_nop 1
	v_cndmask_b32_e32 v22, v22, v23, vcc
	v_rsq_f32_e32 v22, v22
	s_nop 0
	v_mul_f32_e32 v23, 0x45800000, v22
	v_cndmask_b32_e32 v22, v22, v23, vcc
	v_mul_f32_e32 v51, v38, v22
	v_mul_f32_e32 v23, 0xbfb8aa3b, v50
	v_and_b32_e32 v38, 0xffff0000, v24
	v_exp_f32_e32 v23, v23
	v_mul_f32_e32 v24, 0xbfb8aa3b, v38
	v_exp_f32_e32 v24, v24
	v_mul_f32_e32 v39, v39, v22
	v_add_f32_e32 v23, 1.0, v23
	v_rcp_f32_e32 v52, v23
	v_add_f32_e32 v23, 1.0, v24
	v_rcp_f32_e32 v28, v23
	v_mul_f32_e32 v19, v19, v22
	v_pk_mul_f32 v[50:51], v[52:53], v[50:51]
	v_mul_f32_e32 v9, v9, v22
	v_pk_mul_f32 v[28:29], v[28:29], v[38:39]
	v_mul_f32_e32 v23, v50, v51
	v_mul_f32_e32 v50, v28, v29
	v_lshlrev_b32_e32 v28, 16, v25
	v_mul_f32_e32 v24, 0xbfb8aa3b, v28
	v_exp_f32_e32 v38, v24
	v_and_b32_e32 v24, 0xffff0000, v25
	v_mul_f32_e32 v25, 0xbfb8aa3b, v24
	v_exp_f32_e32 v25, v25
	v_add_f32_e32 v38, 1.0, v38
	v_mov_b32_e32 v39, v30
	v_rcp_f32_e32 v38, v38
	v_add_f32_e32 v25, 1.0, v25
	v_rcp_f32_e32 v30, v25
	v_mul_f32_e32 v25, v41, v22
	v_mul_f32_e32 v29, v40, v22
	v_pk_mul_f32 v[28:29], v[38:39], v[28:29]
	v_pk_mul_f32 v[24:25], v[30:31], v[24:25]
	v_mul_f32_e32 v38, v28, v29
	v_mul_f32_e32 v39, v24, v25
	v_lshlrev_b32_e32 v24, 16, v26
	v_mul_f32_e32 v28, 0xbfb8aa3b, v24
	v_exp_f32_e32 v29, v28
	v_and_b32_e32 v28, 0xffff0000, v26
	v_mul_f32_e32 v26, 0xbfb8aa3b, v28
	v_exp_f32_e32 v26, v26
	v_add_f32_e32 v29, 1.0, v29
	v_rcp_f32_e32 v30, v29
	s_waitcnt vmcnt(0)
	v_mov_b32_e32 v31, v32
	v_add_f32_e32 v26, 1.0, v26
	v_rcp_f32_e32 v32, v26
	v_mul_f32_e32 v25, v42, v22
	v_pk_mul_f32 v[24:25], v[30:31], v[24:25]
	v_mul_f32_e32 v29, v43, v22
	v_mul_f32_e32 v30, v24, v25
	v_pk_mul_f32 v[24:25], v[32:33], v[28:29]
	v_mov_b32_e32 v29, v34
	v_mul_f32_e32 v31, v24, v25
	v_lshlrev_b32_e32 v24, 16, v27
	v_mul_f32_e32 v26, 0xbfb8aa3b, v24
	v_exp_f32_e32 v28, v26
	v_and_b32_e32 v26, 0xffff0000, v27
	v_mul_f32_e32 v27, 0xbfb8aa3b, v26
	v_exp_f32_e32 v27, v27
	v_add_f32_e32 v28, 1.0, v28
	v_rcp_f32_e32 v28, v28
	v_mul_f32_e32 v25, v44, v22
	v_add_f32_e32 v27, 1.0, v27
	v_rcp_f32_e32 v34, v27
	v_pk_mul_f32 v[24:25], v[28:29], v[24:25]
	v_mul_f32_e32 v27, v45, v22
	v_mul_f32_e32 v28, v24, v25
	v_pk_mul_f32 v[24:25], v[34:35], v[26:27]
	v_lshl_add_u64 v[32:33], v[36:37], 0, s[0:1]
	v_mul_f32_e32 v27, v24, v25
	v_cvt_pk_bf16_f32 v24, v23, v50
	v_cvt_pk_bf16_f32 v25, v38, v39
	v_cvt_pk_bf16_f32 v26, v30, v31
	v_cvt_pk_bf16_f32 v27, v28, v27
	global_load_dwordx4 v[28:31], v[10:11], off offset:16
	v_lshl_add_u64 v[36:37], v[32:33], 0, v[96:97]
	s_mov_b32 s0, 0x18b00000
	v_add_co_u32_e32 v32, vcc, s0, v36
	v_mul_f32_e32 v40, v46, v22
	s_nop 0
	v_addc_co_u32_e32 v33, vcc, 0, v37, vcc
	global_store_dwordx4 v[32:33], v[24:27], off offset:1024
	global_load_dwordx4 v[24:27], v54, s[4:5] offset:32
	s_nop 0
	global_load_dwordx4 v[32:35], v54, s[4:5] offset:48
	v_mul_f32_e32 v1, v1, v22
	s_waitcnt vmcnt(3)
	v_lshlrev_b32_e32 v39, 16, v28
	v_mul_f32_e32 v23, 0xbfb8aa3b, v39
	v_exp_f32_e32 v23, v23
	v_and_b32_e32 v43, 0xffff0000, v28
	v_add_f32_e32 v23, 1.0, v23
	v_rcp_f32_e32 v41, v23
	v_mul_f32_e32 v23, 0xbfb8aa3b, v43
	v_exp_f32_e32 v23, v23
	s_waitcnt vmcnt(1)
	v_mov_b32_e32 v38, v24
	v_pk_mul_f32 v[38:39], v[40:41], v[38:39]
	v_mov_b32_e32 v42, v25
	v_add_f32_e32 v23, 1.0, v23
	v_lshlrev_b32_e32 v25, 16, v29
	v_mul_f32_e32 v40, v38, v39
	v_rcp_f32_e32 v39, v23
	v_mul_f32_e32 v23, 0xbfb8aa3b, v25
	v_exp_f32_e32 v23, v23
	v_mul_f32_e32 v38, v47, v22
	v_pk_mul_f32 v[38:39], v[38:39], v[42:43]
	v_and_b32_e32 v29, 0xffff0000, v29
	v_add_f32_e32 v23, 1.0, v23
	v_mul_f32_e32 v41, v38, v39
	v_rcp_f32_e32 v39, v23
	v_mul_f32_e32 v23, 0xbfb8aa3b, v29
	v_exp_f32_e32 v23, v23
	v_mul_f32_e32 v38, v48, v22
	v_mov_b32_e32 v24, v26
	v_pk_mul_f32 v[24:25], v[38:39], v[24:25]
	v_add_f32_e32 v23, 1.0, v23
	v_lshlrev_b32_e32 v39, 16, v30
	v_mul_f32_e32 v42, v24, v25
	v_rcp_f32_e32 v25, v23
	v_mul_f32_e32 v23, 0xbfb8aa3b, v39
	v_exp_f32_e32 v23, v23
	v_mul_f32_e32 v24, v49, v22
	v_mov_b32_e32 v28, v27
	v_pk_mul_f32 v[24:25], v[24:25], v[28:29]
	v_add_f32_e32 v23, 1.0, v23
	v_and_b32_e32 v27, 0xffff0000, v30
	v_mul_f32_e32 v43, v24, v25
	v_rcp_f32_e32 v25, v23
	v_mul_f32_e32 v23, 0xbfb8aa3b, v27
	v_exp_f32_e32 v23, v23
	v_mul_f32_e32 v24, v20, v22
	v_mul_f32_e32 v28, v21, v22
	s_waitcnt vmcnt(0)
	v_mov_b32_e32 v26, v33
	v_add_f32_e32 v20, 1.0, v23
	v_rcp_f32_e32 v29, v20
	v_mov_b32_e32 v38, v32
	v_pk_mul_f32 v[24:25], v[24:25], v[38:39]
	v_pk_mul_f32 v[20:21], v[28:29], v[26:27]
	s_nop 0
	v_mul_f32_e32 v26, v20, v21
	v_lshlrev_b32_e32 v20, 16, v31
	v_mul_f32_e32 v21, 0xbfb8aa3b, v20
	v_mul_f32_e32 v23, v24, v25
	v_exp_f32_e32 v24, v21
	v_mov_b32_e32 v21, v34
	v_and_b32_e32 v34, 0xffff0000, v31
	v_mul_f32_e32 v25, 0xbfb8aa3b, v34
	v_exp_f32_e32 v27, v25
	v_add_f32_e32 v24, 1.0, v24
	v_mul_f32_e32 v25, v18, v22
	v_rcp_f32_e32 v24, v24
	v_add_f32_e32 v18, 1.0, v27
	v_rcp_f32_e32 v18, v18
	v_pk_mul_f32 v[20:21], v[24:25], v[20:21]
	s_nop 0
	v_mul_f32_e32 v20, v20, v21
	v_pk_mul_f32 v[18:19], v[18:19], v[34:35]
	v_cvt_pk_bf16_f32 v24, v40, v41
	v_cvt_pk_bf16_f32 v25, v42, v43
	v_cvt_pk_bf16_f32 v26, v23, v26
	s_nop 0
	v_mul_f32_e32 v18, v18, v19
	v_cvt_pk_bf16_f32 v27, v20, v18
	global_load_dwordx4 v[28:31], v[10:11], off offset:32
	v_lshl_add_u64 v[18:19], v[36:37], 0, s[6:7]
	global_store_dwordx4 v[18:19], v[24:27], off offset:16
	global_load_dwordx4 v[24:27], v54, s[4:5] offset:64
	s_nop 0
	global_load_dwordx4 v[32:35], v54, s[4:5] offset:80
	v_mul_f32_e32 v36, v16, v22
	v_readlane_b32 s6, v254, 49
	s_add_i32 s8, s8, s6
	s_cmpk_gt_i32 s8, 0x1ff
	v_readlane_b32 s7, v254, 50
	s_waitcnt vmcnt(3)
	v_lshlrev_b32_e32 v21, 16, v28
	v_mul_f32_e32 v20, 0xbfb8aa3b, v21
	v_exp_f32_e32 v20, v20
	v_and_b32_e32 v39, 0xffff0000, v28
	s_waitcnt vmcnt(1)
	v_mov_b32_e32 v38, v25
	v_and_b32_e32 v25, 0xffff0000, v29
	v_add_f32_e32 v16, 1.0, v20
	v_rcp_f32_e32 v37, v16
	v_mul_f32_e32 v16, 0xbfb8aa3b, v39
	v_exp_f32_e32 v23, v16
	v_mov_b32_e32 v20, v24
	v_pk_mul_f32 v[20:21], v[36:37], v[20:21]
	v_mul_f32_e32 v16, v17, v22
	v_mul_f32_e32 v28, v20, v21
	v_add_f32_e32 v17, 1.0, v23
	v_lshlrev_b32_e32 v21, 16, v29
	v_rcp_f32_e32 v17, v17
	v_mul_f32_e32 v20, 0xbfb8aa3b, v21
	v_exp_f32_e32 v20, v20
	v_pk_mul_f32 v[16:17], v[16:17], v[38:39]
	s_nop 0
	v_mul_f32_e32 v23, v16, v17
	v_mul_f32_e32 v16, v14, v22
	v_add_f32_e32 v14, 1.0, v20
	v_rcp_f32_e32 v17, v14
	v_mul_f32_e32 v14, 0xbfb8aa3b, v25
	v_exp_f32_e32 v24, v14
	v_mov_b32_e32 v20, v26
	v_pk_mul_f32 v[16:17], v[16:17], v[20:21]
	v_mul_f32_e32 v14, v15, v22
	v_mul_f32_e32 v26, v16, v17
	v_add_f32_e32 v15, 1.0, v24
	v_lshlrev_b32_e32 v17, 16, v30
	v_rcp_f32_e32 v15, v15
	v_mul_f32_e32 v16, 0xbfb8aa3b, v17
	v_exp_f32_e32 v16, v16
	v_mov_b32_e32 v24, v27
	v_pk_mul_f32 v[14:15], v[14:15], v[24:25]
	v_and_b32_e32 v21, 0xffff0000, v30
	v_mul_f32_e32 v24, v14, v15
	v_add_f32_e32 v14, 1.0, v16
	v_rcp_f32_e32 v15, v14
	v_mul_f32_e32 v14, 0xbfb8aa3b, v21
	v_exp_f32_e32 v20, v14
	v_mul_f32_e32 v14, v12, v22
	s_waitcnt vmcnt(0)
	v_mov_b32_e32 v16, v32
	v_pk_mul_f32 v[14:15], v[14:15], v[16:17]
	v_add_f32_e32 v12, 1.0, v20
	v_rcp_f32_e32 v17, v12
	v_mul_f32_e32 v16, v13, v22
	v_mov_b32_e32 v20, v33
	v_mul_f32_e32 v25, v14, v15
	v_pk_mul_f32 v[12:13], v[16:17], v[20:21]
	v_mul_f32_e32 v20, v6, v22
	v_mul_f32_e32 v16, v12, v13
	v_lshlrev_b32_e32 v12, 16, v31
	v_mul_f32_e32 v13, 0xbfb8aa3b, v12
	v_exp_f32_e32 v14, v13
	v_mov_b32_e32 v13, v34
	v_and_b32_e32 v34, 0xffff0000, v31
	v_mul_f32_e32 v15, 0xbfb8aa3b, v34
	v_exp_f32_e32 v17, v15
	v_add_f32_e32 v14, 1.0, v14
	v_mul_f32_e32 v15, v8, v22
	v_rcp_f32_e32 v14, v14
	v_add_f32_e32 v8, 1.0, v17
	v_rcp_f32_e32 v8, v8
	v_pk_mul_f32 v[12:13], v[14:15], v[12:13]
	s_nop 0
	v_mul_f32_e32 v15, v12, v13
	v_pk_mul_f32 v[8:9], v[8:9], v[34:35]
	v_cvt_pk_bf16_f32 v12, v28, v23
	v_cvt_pk_bf16_f32 v13, v26, v24
	v_cvt_pk_bf16_f32 v14, v25, v16
	s_nop 0
	v_mul_f32_e32 v8, v8, v9
	v_cvt_pk_bf16_f32 v15, v15, v8
	global_load_dwordx4 v[8:11], v[10:11], off offset:48
	s_waitcnt vmcnt(0)
	v_lshlrev_b32_e32 v17, 16, v8
	global_store_dwordx4 v[18:19], v[12:15], off offset:32
	global_load_dwordx4 v[12:15], v54, s[4:5] offset:96
	s_nop 0
	global_load_dwordx4 v[24:27], v54, s[4:5] offset:112
	v_mul_f32_e32 v16, 0xbfb8aa3b, v17
	v_exp_f32_e32 v16, v16
	v_and_b32_e32 v29, 0xffff0000, v8
	v_add_f32_e32 v6, 1.0, v16
	v_rcp_f32_e32 v21, v6
	v_mul_f32_e32 v6, 0xbfb8aa3b, v29
	v_exp_f32_e32 v8, v6
	v_mul_f32_e32 v6, v7, v22
	v_add_f32_e32 v7, 1.0, v8
	v_rcp_f32_e32 v7, v7
	s_waitcnt vmcnt(1)
	v_mov_b32_e32 v28, v13
	v_lshlrev_b32_e32 v13, 16, v9
	v_mul_f32_e32 v8, 0xbfb8aa3b, v13
	v_exp_f32_e32 v8, v8
	v_mov_b32_e32 v16, v12
	v_pk_mul_f32 v[16:17], v[20:21], v[16:17]
	v_pk_mul_f32 v[6:7], v[6:7], v[28:29]
	v_mul_f32_e32 v16, v16, v17
	v_mul_f32_e32 v17, v6, v7
	v_mul_f32_e32 v6, v4, v22
	v_add_f32_e32 v4, 1.0, v8
	v_and_b32_e32 v9, 0xffff0000, v9
	v_rcp_f32_e32 v7, v4
	v_mul_f32_e32 v4, 0xbfb8aa3b, v9
	v_exp_f32_e32 v8, v4
	v_mov_b32_e32 v12, v14
	v_pk_mul_f32 v[6:7], v[6:7], v[12:13]
	v_mul_f32_e32 v4, v5, v22
	v_mul_f32_e32 v12, v6, v7
	v_add_f32_e32 v5, 1.0, v8
	v_lshlrev_b32_e32 v7, 16, v10
	v_rcp_f32_e32 v5, v5
	v_mul_f32_e32 v6, 0xbfb8aa3b, v7
	v_exp_f32_e32 v6, v6
	v_mov_b32_e32 v8, v15
	v_pk_mul_f32 v[4:5], v[4:5], v[8:9]
	v_and_b32_e32 v9, 0xffff0000, v10
	v_mul_f32_e32 v13, v4, v5
	v_add_f32_e32 v4, 1.0, v6
	v_rcp_f32_e32 v5, v4
	v_mul_f32_e32 v4, 0xbfb8aa3b, v9
	v_exp_f32_e32 v8, v4
	v_mul_f32_e32 v4, v2, v22
	s_waitcnt vmcnt(0)
	v_mov_b32_e32 v6, v24
	v_pk_mul_f32 v[4:5], v[4:5], v[6:7]
	v_add_f32_e32 v2, 1.0, v8
	v_rcp_f32_e32 v7, v2
	v_mul_f32_e32 v6, v3, v22
	v_mov_b32_e32 v8, v25
	v_mul_f32_e32 v10, v4, v5
	v_pk_mul_f32 v[2:3], v[6:7], v[8:9]
	s_nop 0
	v_mul_f32_e32 v6, v2, v3
	v_lshlrev_b32_e32 v2, 16, v11
	v_mul_f32_e32 v3, 0xbfb8aa3b, v2
	v_exp_f32_e32 v4, v3
	v_mov_b32_e32 v3, v26
	v_and_b32_e32 v26, 0xffff0000, v11
	v_mul_f32_e32 v5, 0xbfb8aa3b, v26
	v_exp_f32_e32 v7, v5
	v_add_f32_e32 v4, 1.0, v4
	v_rcp_f32_e32 v4, v4
	v_mul_f32_e32 v5, v0, v22
	v_add_f32_e32 v0, 1.0, v7
	v_rcp_f32_e32 v0, v0
	v_pk_mul_f32 v[2:3], v[4:5], v[2:3]
	v_pk_mul_f32 v[0:1], v[0:1], v[26:27]
	v_mul_f32_e32 v3, v2, v3
	v_mul_f32_e32 v4, v0, v1
	v_cvt_pk_bf16_f32 v0, v16, v17
	v_cvt_pk_bf16_f32 v1, v12, v13
	v_cvt_pk_bf16_f32 v2, v10, v6
	v_cvt_pk_bf16_f32 v3, v3, v4
	global_store_dwordx4 v[18:19], v[0:3], off offset:48
	s_barrier
	s_cbranch_scc1 .LBB0_988
